# speedup vs baseline: 1.0526x; 1.0526x over previous
.Lq_go_1:
	ds_read_b128 v[228:231], v5 offset:16384
	ds_read_b128 v[232:235], v5 offset:16896
	ds_read_b128 v[236:239], v5 offset:17408
	ds_read_b128 v[240:243], v5 offset:17920
	v_mul_f32_e32 v244, v148, v152
	v_mul_f32_e32 v250, v149, v153
	v_mul_f32_e64 v245, -v152, v152
	v_mul_f32_e64 v251, -v153, v153
	v_add_f32_e32 v246, v148, v152
	v_add_f32_e32 v252, v149, v153
	v_fma_f32 v245, -v148, v148, v245
	v_fma_f32 v251, -v149, v149, v251
	v_fma_f32 v247, v10, v246, v11
	v_fma_f32 v253, v10, v252, v11
	v_fma_f32 v246, v13, v160, v14
	v_fma_f32 v252, v13, v161, v14
	v_fma_f32 v248, v12, v156, v245
	v_fma_f32 v254, v12, v157, v251
	v_fma_f32 v249, 2.0, v244, v247
	v_fma_f32 v255, 2.0, v250, v253
	v_sub_f32_e32 v247, v247, v245
	v_sub_f32_e32 v253, v253, v251
	v_fma_f32 v246, -2.0, v244, v246
	v_fma_f32 v252, -2.0, v250, v252
	v_mul_f32_e32 v247, v247, v248
	v_mul_f32_e32 v253, v253, v254
	v_rcp_f32_e32 v247, v247
	v_rcp_f32_e32 v253, v253
	v_mul_f32_e32 v249, v249, v246
	v_mul_f32_e32 v255, v255, v252
	v_fma_f32 v19, v249, v247, v19
	v_fma_f32 v19, v255, v253, v19
	v_mul_f32_e32 v244, v150, v154
	v_mul_f32_e32 v250, v151, v155
	v_mul_f32_e64 v245, -v154, v154
	v_mul_f32_e64 v251, -v155, v155
	v_add_f32_e32 v246, v150, v154
	v_add_f32_e32 v252, v151, v155
	v_fma_f32 v245, -v150, v150, v245
	v_fma_f32 v251, -v151, v151, v251
	v_fma_f32 v247, v10, v246, v11
	v_fma_f32 v253, v10, v252, v11
	v_fma_f32 v246, v13, v162, v14
	v_fma_f32 v252, v13, v163, v14
	v_fma_f32 v248, v12, v158, v245
	v_fma_f32 v254, v12, v159, v251
	v_fma_f32 v249, 2.0, v244, v247
	v_fma_f32 v255, 2.0, v250, v253
	v_sub_f32_e32 v247, v247, v245
	v_sub_f32_e32 v253, v253, v251
	v_fma_f32 v246, -2.0, v244, v246
	v_fma_f32 v252, -2.0, v250, v252
	v_mul_f32_e32 v247, v247, v248
	v_mul_f32_e32 v253, v253, v254
	v_rcp_f32_e32 v247, v247
	v_rcp_f32_e32 v253, v253
	v_mul_f32_e32 v249, v249, v246
	v_mul_f32_e32 v255, v255, v252
	v_fma_f32 v20, v249, v247, v20
	v_fma_f32 v20, v255, v253, v20
	s_waitcnt lgkmcnt(0)
	v_mfma_f32_16x16x32_f16 v[148:151], v[28:31], v[228:231], 0
	v_mfma_f32_16x16x32_f16 v[152:155], v[28:31], v[232:235], 0
	v_mfma_f32_16x16x32_f16 v[156:159], v[28:31], v[236:239], v[0:3]
	v_mfma_f32_16x16x32_f16 v[160:163], v[28:31], v[240:243], 0
	v_mfma_f32_16x16x32_f16 v[148:151], v[32:35], v[100:103], v[148:151]
	v_mfma_f32_16x16x32_f16 v[152:155], v[32:35], v[108:111], v[152:155]
	v_mfma_f32_16x16x32_f16 v[156:159], v[32:35], v[116:119], v[156:159]
	v_mfma_f32_16x16x32_f16 v[160:163], v[32:35], v[124:127], v[160:163]
	v_mul_f32_e32 v244, v132, v136
	v_mul_f32_e32 v250, v133, v137
	v_mul_f32_e64 v245, -v136, v136
	v_mul_f32_e64 v251, -v137, v137
	v_add_f32_e32 v246, v132, v136
	v_add_f32_e32 v252, v133, v137
	v_fma_f32 v245, -v132, v132, v245
	v_fma_f32 v251, -v133, v133, v251
	v_fma_f32 v247, v10, v246, v11
	v_fma_f32 v253, v10, v252, v11
	v_fma_f32 v246, v13, v144, v14
	v_fma_f32 v252, v13, v145, v14
	v_fma_f32 v248, v12, v140, v245
	v_fma_f32 v254, v12, v141, v251
	v_fma_f32 v249, 2.0, v244, v247
	v_fma_f32 v255, 2.0, v250, v253
	v_sub_f32_e32 v247, v247, v245
	v_sub_f32_e32 v253, v253, v251
	v_fma_f32 v246, -2.0, v244, v246
	v_fma_f32 v252, -2.0, v250, v252
	v_mul_f32_e32 v247, v247, v248
	v_mul_f32_e32 v253, v253, v254
	v_rcp_f32_e32 v247, v247
	v_rcp_f32_e32 v253, v253
	v_mul_f32_e32 v249, v249, v246
	v_mul_f32_e32 v255, v255, v252
	v_fma_f32 v19, v249, v247, v19
	v_fma_f32 v19, v255, v253, v19
	v_mul_f32_e32 v244, v134, v138
	v_mul_f32_e32 v250, v135, v139
	v_mul_f32_e64 v245, -v138, v138
	v_mul_f32_e64 v251, -v139, v139
	v_add_f32_e32 v246, v134, v138
	v_add_f32_e32 v252, v135, v139
	v_fma_f32 v245, -v134, v134, v245
	v_fma_f32 v251, -v135, v135, v251
	v_fma_f32 v247, v10, v246, v11
	v_fma_f32 v253, v10, v252, v11
	v_fma_f32 v246, v13, v146, v14
	v_fma_f32 v252, v13, v147, v14
	v_fma_f32 v248, v12, v142, v245
	v_fma_f32 v254, v12, v143, v251
	v_fma_f32 v249, 2.0, v244, v247
	v_fma_f32 v255, 2.0, v250, v253
	v_sub_f32_e32 v247, v247, v245
	v_sub_f32_e32 v253, v253, v251
	v_fma_f32 v246, -2.0, v244, v246
	v_fma_f32 v252, -2.0, v250, v252
	v_mul_f32_e32 v247, v247, v248
	v_mul_f32_e32 v253, v253, v254
	v_rcp_f32_e32 v247, v247
	v_rcp_f32_e32 v253, v253
	v_mul_f32_e32 v249, v249, v246
	v_mul_f32_e32 v255, v255, v252
	v_fma_f32 v20, v249, v247, v20
	v_fma_f32 v20, v255, v253, v20
	v_mul_f32_e32 v244, v148, v152
	v_mul_f32_e32 v250, v149, v153
	v_mul_f32_e64 v245, -v152, v152
	v_mul_f32_e64 v251, -v153, v153
	v_add_f32_e32 v246, v148, v152
	v_add_f32_e32 v252, v149, v153
	v_fma_f32 v245, -v148, v148, v245
	v_fma_f32 v251, -v149, v149, v251
	v_fma_f32 v247, v10, v246, v11
	v_fma_f32 v253, v10, v252, v11
	v_fma_f32 v246, v13, v160, v14
	v_fma_f32 v252, v13, v161, v14
	v_fma_f32 v248, v12, v156, v245
	v_fma_f32 v254, v12, v157, v251
	v_fma_f32 v249, 2.0, v244, v247
	v_fma_f32 v255, 2.0, v250, v253
	v_sub_f32_e32 v247, v247, v245
	v_sub_f32_e32 v253, v253, v251
	v_fma_f32 v246, -2.0, v244, v246
	v_fma_f32 v252, -2.0, v250, v252
	v_mul_f32_e32 v247, v247, v248
	v_mul_f32_e32 v253, v253, v254
	v_rcp_f32_e32 v247, v247
	v_rcp_f32_e32 v253, v253
	v_mul_f32_e32 v249, v249, v246
	v_mul_f32_e32 v255, v255, v252
	v_mul_f32_e32 v249, v249, v247
	v_mul_f32_e32 v255, v255, v253
	v_fma_f32 v19, v249, v15, v19
	v_fma_f32 v19, v255, v16, v19
	v_mul_f32_e32 v244, v150, v154
	v_mul_f32_e32 v250, v151, v155
	v_mul_f32_e64 v245, -v154, v154
	v_mul_f32_e64 v251, -v155, v155
	v_add_f32_e32 v246, v150, v154
	v_add_f32_e32 v252, v151, v155
	v_fma_f32 v245, -v150, v150, v245
	v_fma_f32 v251, -v151, v151, v251
	v_fma_f32 v247, v10, v246, v11
	v_fma_f32 v253, v10, v252, v11
	v_fma_f32 v246, v13, v162, v14
	v_fma_f32 v252, v13, v163, v14
	v_fma_f32 v248, v12, v158, v245
	v_fma_f32 v254, v12, v159, v251
	v_fma_f32 v249, 2.0, v244, v247
	v_fma_f32 v255, 2.0, v250, v253
	v_sub_f32_e32 v247, v247, v245
	v_sub_f32_e32 v253, v253, v251
	v_fma_f32 v246, -2.0, v244, v246
	v_fma_f32 v252, -2.0, v250, v252
	v_mul_f32_e32 v247, v247, v248
	v_mul_f32_e32 v253, v253, v254
	v_rcp_f32_e32 v247, v247
	v_rcp_f32_e32 v253, v253
	v_mul_f32_e32 v249, v249, v246
	v_mul_f32_e32 v255, v255, v252
	v_mul_f32_e32 v249, v249, v247
	v_mul_f32_e32 v255, v255, v253
	v_fma_f32 v20, v249, v17, v20
	v_fma_f32 v20, v255, v18, v20
	s_setprio 0
	v_mfma_f32_16x16x32_f16 v[132:135], v[36:39], v[24:27], 0
	v_mfma_f32_16x16x32_f16 v[136:139], v[40:43], v[24:27], 0
	v_mfma_f32_16x16x32_f16 v[140:143], v[44:47], v[24:27], 0
	v_mfma_f32_16x16x32_f16 v[144:147], v[48:51], v[24:27], 0
	v_mfma_f32_16x16x32_f16 v[148:151], v[52:55], v[24:27], 0
	v_mfma_f32_16x16x32_f16 v[152:155], v[56:59], v[24:27], 0
	v_mfma_f32_16x16x32_f16 v[156:159], v[60:63], v[24:27], 0
	v_mfma_f32_16x16x32_f16 v[160:163], v[64:67], v[24:27], 0
	s_nop 1
	v_cvt_pk_f16_f32 v100, v132, v136
	s_nop 0
	v_cvt_pk_f16_f32 v101, v140, v144
	v_cvt_pk_f16_f32 v102, v133, v137
	v_cvt_pk_f16_f32 v103, v141, v145
	v_cvt_pk_f16_f32 v104, v134, v138
	v_cvt_pk_f16_f32 v105, v142, v146
	v_cvt_pk_f16_f32 v106, v135, v139
	v_cvt_pk_f16_f32 v107, v143, v147
	v_mfma_f32_16x16x32_f16 v[132:135], v[68:71], v[24:27], 0
	v_mfma_f32_16x16x32_f16 v[136:139], v[72:75], v[24:27], 0
	v_mfma_f32_16x16x32_f16 v[140:143], v[76:79], v[24:27], 0
	v_mfma_f32_16x16x32_f16 v[144:147], v[80:83], v[24:27], 0
	v_cvt_pk_f16_f32 v108, v148, v152
	v_cvt_pk_f16_f32 v109, v156, v160
	v_cvt_pk_f16_f32 v110, v149, v153
	v_cvt_pk_f16_f32 v111, v157, v161
	v_cvt_pk_f16_f32 v112, v150, v154
	v_cvt_pk_f16_f32 v113, v158, v162
	v_cvt_pk_f16_f32 v114, v151, v155
	v_cvt_pk_f16_f32 v115, v159, v163
	v_mfma_f32_16x16x32_f16 v[148:151], v[84:87], v[24:27], 0
	v_mfma_f32_16x16x32_f16 v[152:155], v[88:91], v[24:27], 0
	v_mfma_f32_16x16x32_f16 v[156:159], v[92:95], v[24:27], 0
	v_mfma_f32_16x16x32_f16 v[160:163], v[96:99], v[24:27], 0
	v_cvt_pk_f16_f32 v116, v132, v136
	v_cvt_pk_f16_f32 v117, v140, v144
	v_cvt_pk_f16_f32 v118, v133, v137
	v_cvt_pk_f16_f32 v119, v141, v145
	v_cvt_pk_f16_f32 v120, v134, v138
	v_cvt_pk_f16_f32 v121, v142, v146
	v_cvt_pk_f16_f32 v122, v135, v139
	v_cvt_pk_f16_f32 v123, v143, v147
	v_cvt_pk_f16_f32 v124, v148, v152
	v_cvt_pk_f16_f32 v125, v156, v160
	v_cvt_pk_f16_f32 v126, v149, v153
	v_cvt_pk_f16_f32 v127, v157, v161
	v_cvt_pk_f16_f32 v128, v150, v154
	v_cvt_pk_f16_f32 v129, v158, v162
	v_cvt_pk_f16_f32 v130, v151, v155
	v_cvt_pk_f16_f32 v131, v159, v163
	s_mov_b64 exec, s[38:39]
	ds_write_b128 v4, v[104:107] offset:32768
	ds_write_b128 v4, v[112:115] offset:33280
	ds_write_b128 v4, v[120:123] offset:33792
	ds_write_b128 v4, v[128:131] offset:34304
	s_mov_b64 exec, -1
	v_mfma_f32_16x16x32_f16 v[132:135], v[24:27], v[100:103], 0
	v_mfma_f32_16x16x32_f16 v[136:139], v[24:27], v[108:111], 0
	v_mfma_f32_16x16x32_f16 v[140:143], v[24:27], v[116:119], v[0:3]
	v_mfma_f32_16x16x32_f16 v[144:147], v[24:27], v[124:127], 0
	v_mfma_f32_16x16x32_f16 v[148:151], v[28:31], v[100:103], 0
	v_mfma_f32_16x16x32_f16 v[152:155], v[28:31], v[108:111], 0
	v_mfma_f32_16x16x32_f16 v[156:159], v[28:31], v[116:119], v[0:3]
	v_mfma_f32_16x16x32_f16 v[160:163], v[28:31], v[124:127], 0
	v_mfma_f32_16x16x32_f16 v[148:151], v[32:35], v[104:107], v[148:151]
	v_mfma_f32_16x16x32_f16 v[152:155], v[32:35], v[112:115], v[152:155]
	v_mfma_f32_16x16x32_f16 v[156:159], v[32:35], v[120:123], v[156:159]
	v_mfma_f32_16x16x32_f16 v[160:163], v[32:35], v[128:131], v[160:163]
	s_waitcnt lgkmcnt(0)
	ds_write_b32 v6, v6 offset:64
	ds_read_b32 v9, v7 offset:64
	v_mul_f32_e32 v244, v132, v136
	v_mul_f32_e32 v250, v133, v137
	v_mul_f32_e64 v245, -v136, v136
	v_mul_f32_e64 v251, -v137, v137
	v_add_f32_e32 v246, v132, v136
	v_add_f32_e32 v252, v133, v137
	v_fma_f32 v245, -v132, v132, v245
	v_fma_f32 v251, -v133, v133, v251
	v_fma_f32 v247, v10, v246, v11
	v_fma_f32 v253, v10, v252, v11
	v_fma_f32 v246, v13, v144, v14
	v_fma_f32 v252, v13, v145, v14
	v_fma_f32 v248, v12, v140, v245
	v_fma_f32 v254, v12, v141, v251
	v_fma_f32 v249, 2.0, v244, v247
	v_fma_f32 v255, 2.0, v250, v253
	v_sub_f32_e32 v247, v247, v245
	v_sub_f32_e32 v253, v253, v251
	v_fma_f32 v246, -2.0, v244, v246
	v_fma_f32 v252, -2.0, v250, v252
	v_mul_f32_e32 v247, v247, v248
	v_mul_f32_e32 v253, v253, v254
	v_rcp_f32_e32 v247, v247
	v_rcp_f32_e32 v253, v253
	v_mul_f32_e32 v249, v249, v246
	v_mul_f32_e32 v255, v255, v252
	v_fma_f32 v19, v249, v247, v19
	v_fma_f32 v19, v255, v253, v19
	v_mul_f32_e32 v244, v134, v138
	v_mul_f32_e32 v250, v135, v139
	v_mul_f32_e64 v245, -v138, v138
	v_mul_f32_e64 v251, -v139, v139
	v_add_f32_e32 v246, v134, v138
	v_add_f32_e32 v252, v135, v139
	v_fma_f32 v245, -v134, v134, v245
	v_fma_f32 v251, -v135, v135, v251
	v_fma_f32 v247, v10, v246, v11
	v_fma_f32 v253, v10, v252, v11
	v_fma_f32 v246, v13, v146, v14
	v_fma_f32 v252, v13, v147, v14
	v_fma_f32 v248, v12, v142, v245
	v_fma_f32 v254, v12, v143, v251
	v_fma_f32 v249, 2.0, v244, v247
	v_fma_f32 v255, 2.0, v250, v253
	v_sub_f32_e32 v247, v247, v245
	v_sub_f32_e32 v253, v253, v251
	v_fma_f32 v246, -2.0, v244, v246
	v_fma_f32 v252, -2.0, v250, v252
	v_mul_f32_e32 v247, v247, v248
	v_mul_f32_e32 v253, v253, v254
	v_rcp_f32_e32 v247, v247
	v_rcp_f32_e32 v253, v253
	v_mul_f32_e32 v249, v249, v246
	v_mul_f32_e32 v255, v255, v252
	v_fma_f32 v20, v249, v247, v20
	v_fma_f32 v20, v255, v253, v20
	v_mfma_f32_16x16x32_f16 v[132:135], v[24:27], v[104:107], 0
	v_mfma_f32_16x16x32_f16 v[136:139], v[24:27], v[112:115], 0
	v_mfma_f32_16x16x32_f16 v[140:143], v[24:27], v[120:123], v[0:3]
	v_mfma_f32_16x16x32_f16 v[144:147], v[24:27], v[128:131], 0
	s_waitcnt lgkmcnt(0)
	v_cmp_ne_u32_e32 vcc, 0, v9
	s_cbranch_vccnz .Lq_go_2
